# v17 + od_nat and att GEMMs both walk their units in reverse order
# speedup vs baseline: 1.0018x; 1.0007x over previous
.LBB0_189:
	s_cmp_eq_u32 s54, 15
	v_writelane_b32 v252, s35, 12
	s_cselect_b64 s[0:1], -1, 0
	v_writelane_b32 v252, s0, 13
	s_cmp_eq_u32 s54, 14
	v_mov_b32_e32 v228, 1
	v_writelane_b32 v252, s1, 14
	s_cselect_b64 s[0:1], -1, 0
	v_writelane_b32 v252, s0, 15
	s_cmp_eq_u32 s54, 13
	v_mov_b32_e32 v222, 0x7f7f7f7f
	v_writelane_b32 v252, s1, 16
	s_cselect_b64 s[0:1], -1, 0
	v_writelane_b32 v252, s0, 17
	s_cmp_eq_u32 s54, 12
	v_mov_b32_e32 v186, 0x358637bd
	v_writelane_b32 v252, s1, 18
	s_cselect_b64 s[0:1], -1, 0
	v_writelane_b32 v252, s0, 19
	s_cmp_eq_u32 s54, 11
	v_mov_b32_e32 v224, 0x42800000
	v_writelane_b32 v252, s1, 20
	s_cselect_b64 s[0:1], -1, 0
	v_writelane_b32 v252, s0, 21
	s_cmp_eq_u32 s54, 10
	v_not_b32_e32 v225, 63
	v_writelane_b32 v252, s1, 22
	s_cselect_b64 s[0:1], -1, 0
	v_writelane_b32 v252, s0, 23
	s_cmp_eq_u32 s54, 9
	v_mov_b64_e32 v[230:231], 0x3ff
	v_writelane_b32 v252, s1, 24
	s_cselect_b64 s[0:1], -1, 0
	v_writelane_b32 v252, s0, 25
	s_cmp_eq_u32 s54, 8
	v_mov_b64_e32 v[248:249], 0x400
	v_writelane_b32 v252, s1, 26
	s_cselect_b64 s[0:1], -1, 0
	v_writelane_b32 v252, s0, 27
	s_cmp_eq_u32 s54, 7
	v_mov_b64_e32 v[250:251], 0x1ff
	v_writelane_b32 v252, s1, 28
	s_cselect_b64 s[0:1], -1, 0
	v_writelane_b32 v252, s0, 29
	s_cmp_eq_u32 s54, 6
	v_mov_b32_e32 v187, 0x4ba00000
	v_writelane_b32 v252, s1, 30
	s_cselect_b64 s[0:1], -1, 0
	v_writelane_b32 v252, s0, 31
	s_cmp_eq_u32 s54, 5
	v_mov_b32_e32 v223, 0x4b200000
	v_writelane_b32 v252, s1, 32
	s_cselect_b64 s[0:1], -1, 0
	v_writelane_b32 v252, s0, 33
	s_cmp_eq_u32 s54, 4
	v_mov_b32_e32 v229, 0xf149f2ca
	v_writelane_b32 v252, s1, 34
	s_cselect_b64 s[0:1], -1, 0
	v_writelane_b32 v252, s0, 35
	s_cmp_eq_u32 s54, 3
	s_mov_b32 s37, 0xefa18f08
	v_writelane_b32 v252, s1, 36
	s_cselect_b64 s[0:1], -1, 0
	v_writelane_b32 v252, s0, 37
	s_cmp_eq_u32 s54, 2
	s_mov_b32 s23, 0xc0e00000
	v_writelane_b32 v252, s1, 38
	s_cselect_b64 s[0:1], -1, 0
	v_writelane_b32 v252, s0, 39
	s_cmp_eq_u32 s54, 1
	s_mov_b32 s36, 0x3fb8aa3b
	v_writelane_b32 v252, s1, 40
	s_cselect_b64 s[0:1], -1, 0
	v_writelane_b32 v252, s0, 41
	s_cmp_eq_u32 s54, 0
	s_nop 0
	v_writelane_b32 v252, s1, 42
	s_cselect_b64 s[0:1], -1, 0
	v_writelane_b32 v252, s0, 43
	s_nop 1
	v_writelane_b32 v252, s1, 44
	s_lshl_b32 s0, s54, 6
	s_cmpk_lt_i32 s88, 0x100
	v_writelane_b32 v252, s0, 45
	s_cselect_b64 s[0:1], -1, 0
	v_writelane_b32 v252, s0, 46
	s_cmpk_lt_i32 s88, 0x800
	s_nop 0
	v_writelane_b32 v252, s1, 47
	s_cselect_b64 s[0:1], -1, 0
	v_writelane_b32 v252, s0, 48
	s_nop 1
	v_writelane_b32 v252, s1, 49
	s_ashr_i32 s0, s88, 31
	v_writelane_b32 v252, s0, 50
	s_lshr_b32 s0, s0, 29
	s_add_i32 s0, s88, s0
	v_readlane_b32 s1, v252, 4
	s_ashr_i32 s21, s0, 3
	s_and_b32 s0, s0, -8
	s_lshr_b32 s3, s1, 8
	s_sub_i32 s22, s88, s0
	v_writelane_b32 v252, s3, 51
	s_bfe_u32 s1, s1, 0x20006
	s_lshl_b32 s0, s22, 8
	v_writelane_b32 v252, s1, 52
	s_ashr_i32 s1, s2, 31
	s_cmpk_lt_i32 s88, 0x400
	v_writelane_b32 v252, s1, 53
	s_waitcnt lgkmcnt(0)
	s_cselect_b64 s[4:5], -1, 0
	v_writelane_b32 v252, s4, 54
	s_max_i32 s1, s2, 2
	s_and_b32 s6, s88, 1
	v_writelane_b32 v252, s5, 55
	s_lshr_b32 s4, s1, 1
	v_readlane_b32 s1, v252, 11
	s_and_b32 s1, s1, -16
	s_or_b32 s5, s1, s6
	v_writelane_b32 v252, s5, 56
	s_lshl_b32 s3, s22, 7
	v_writelane_b32 v252, s4, 57
	s_min_i32 s4, s4, 0x80
	s_cmp_gt_i32 s4, s88
	s_cselect_b64 s[4:5], -1, 0
	v_writelane_b32 v252, s4, 58
	s_nop 1
	v_writelane_b32 v252, s5, 59
	s_ashr_i32 s4, s1, 1
	s_ashr_i32 s5, s4, 31
	s_lshl_b64 s[8:9], s[4:5], 19
	v_writelane_b32 v252, s8, 60
	s_lshl_b64 s[4:5], s[4:5], 17
	s_lshl_b32 s1, s6, 17
	v_writelane_b32 v252, s9, 61
	v_writelane_b32 v252, s4, 62
	s_nop 1
	v_writelane_b32 v252, s5, 63
	s_lshr_b32 s4, s2, 31
	s_add_i32 s4, s2, s4
	s_ashr_i32 s4, s4, 1
	s_cmp_gt_i32 s2, 1
	s_cselect_b32 s4, s4, 1
	s_sub_i32 s8, s2, s4
	s_sub_i32 s9, s88, s4
	s_cmp_ge_i32 s88, s4
	s_cselect_b64 s[4:5], -1, 0
	s_and_b64 s[6:7], s[4:5], exec
	s_cselect_b32 s10, s8, 1
	s_cselect_b32 s11, s9, 0
	s_cmp_lt_i32 s2, 2
	s_cselect_b64 s[6:7], -1, 0
	s_and_b64 s[8:9], s[6:7], exec
	s_cselect_b32 s8, 1, s10
	s_cselect_b32 s9, 0, s11
	s_or_b64 s[4:5], s[6:7], s[4:5]
	s_and_b64 s[4:5], s[4:5], exec
	s_cselect_b32 s24, 0x200, 0
	s_cmp_lt_i32 s9, s24
	s_cselect_b64 s[4:5], -1, 0
	v_writelane_b32 v253, s4, 0
	s_lshr_b32 s16, s24, 3
	s_or_b32 s17, s16, 1
	v_writelane_b32 v253, s5, 1
	s_ashr_i32 s4, s9, 31
	v_writelane_b32 v253, s4, 2
	s_lshr_b32 s4, s4, 29
	s_add_i32 s4, s9, s4
	s_ashr_i32 s6, s4, 3
	s_and_b32 s4, s4, -8
	v_writelane_b32 v253, s9, 3
	s_sub_i32 s7, s9, s4
	s_ashr_i32 s4, s8, 31
	s_lshl_b32 s34, s2, 4
	v_writelane_b32 v253, s8, 4
	s_cmpk_lt_i32 s88, 0x200
	v_writelane_b32 v253, s4, 5
	s_cselect_b64 s[4:5], -1, 0
	v_writelane_b32 v253, s4, 6
	s_mul_i32 s10, s22, 0x41
	s_mul_i32 s11, s22, 5
	v_writelane_b32 v253, s5, 7
	s_lshl_b32 s4, s22, 6
	s_cmpk_lt_i32 s88, 0x180
	s_cselect_b64 s[8:9], -1, 0
	v_writelane_b32 v253, s8, 8
	s_cmp_lt_i32 s88, 32
	s_nop 0
	v_writelane_b32 v253, s9, 9
	s_cselect_b64 s[8:9], -1, 0
	v_writelane_b32 v253, s8, 10
	s_lshl_b32 s5, s22, 2
	s_nop 0
	v_writelane_b32 v253, s9, 11
	s_lshl_b32 s8, s88, 9
	v_writelane_b32 v253, s8, 12
	s_lshl_b32 s8, s2, 9
	v_writelane_b32 v253, s8, 13
	s_cmp_lt_i32 s22, 0
	s_mul_i32 s8, s22, 0x101
	s_mul_i32 s9, s22, 0x81
	s_cselect_b32 s0, s8, s0
	s_cselect_b32 s8, s9, s3
	s_cselect_b32 s9, s10, s4
	s_cselect_b32 s10, 49, 48
	s_cselect_b32 s3, s11, s5
	s_add_i32 s0, s0, s21
	s_sub_i32 s0, 0x7ff, s0
	s_ashr_i32 s4, s0, 31
	s_lshr_b32 s4, s4, 25
	s_add_i32 s4, s0, s4
	s_ashr_i32 s5, s0, 5
	s_and_b32 s4, s0, 31
	s_and_b32 s11, s4, 1
	s_lshr_b32 s12, s4, 1
	s_nop 0
	s_nop 0
	s_nop 0
	s_nop 0
	s_nop 0
	s_lshl_b32 s5, s5, 1
	s_nop 0
	s_nop 0
	s_add_i32 s8, s8, s21
	s_add_i32 s26, s5, s11
	s_mov_b32 s4, s12
	s_ashr_i32 s11, s8, 31
	v_writelane_b32 v253, s4, 14
	s_lshr_b32 s4, s11, 22
	s_add_i32 s4, s8, s4
	s_ashr_i32 s5, s4, 10
	s_and_b32 s4, s4, 0xfc00
	s_sub_i32 s4, s8, s4
	s_mov_b32 s0, s12
	s_sext_i32_i16 s12, s4
	s_bfe_u32 s12, s12, 0x3001c
	s_add_i32 s12, s4, s12
	s_sext_i32_i16 s13, s12
	s_and_b32 s12, s12, 0xfff8
	s_sub_i32 s12, s4, s12
	s_lshl_b32 s5, s5, 3
	s_sext_i32_i16 s12, s12
	s_lshr_b32 s4, s13, 3
	s_add_i32 s12, s5, s12
	s_ashr_i32 s5, s13, 3
	v_writelane_b32 v253, s5, 15
	s_bfe_i64 s[4:5], s[4:5], 0x100000
	s_lshl_b64 s[4:5], s[4:5], 18
	v_writelane_b32 v253, s4, 16
	s_ashr_i32 s13, s12, 31
	s_mul_i32 s10, s22, s10
	v_writelane_b32 v253, s5, 17
	s_mov_b32 s4, s12
	v_writelane_b32 v253, s4, 18
	s_nop 1
	v_writelane_b32 v253, s5, 19
	s_lshl_b64 s[4:5], s[12:13], 18
	v_writelane_b32 v253, s4, 20
	s_cmp_lt_i32 s7, 0
	s_cselect_b32 s12, s17, s16
	v_writelane_b32 v253, s5, 21
	s_lshr_b32 s4, s11, 28
	s_add_i32 s4, s8, s4
	s_and_b32 s5, s4, 0xfff0
	s_sub_i32 s5, s8, s5
	s_bfe_i32 s13, s5, 0x80000
	s_bfe_u32 s13, s13, 0x3000c
	s_mul_i32 s7, s12, s7
	s_add_i32 s13, s5, s13
	s_add_i32 s6, s7, s6
	s_sub_i32 s6, 0x1ff, s6
	s_add_i32 s7, s9, s21
	v_writelane_b32 v253, s16, 22
	s_and_b32 s16, s13, 0xf8
	s_ashr_i32 s9, s7, 31
	s_sub_i32 s16, s5, s16
	s_ashr_i32 s4, s4, 4
	s_lshr_b32 s9, s9, 27
	s_lshl_b32 s4, s4, 3
	s_sext_i32_i8 s5, s16
	s_add_i32 s9, s7, s9
	s_add_i32 s28, s4, s5
	s_and_b32 s12, s9, 0xffe0
	s_ashr_i32 s4, s28, 5
	s_sub_i32 s7, s7, s12
	s_ashr_i32 s5, s4, 31
	s_lshl_b32 s16, s16, 10
	s_bfe_i32 s12, s7, 0x80000
	s_and_b32 s16, s16, 0x1c00
	s_lshl_b64 s[4:5], s[4:5], 13
	s_bfe_u32 s12, s12, 0x3000c
	s_or_b32 s4, s4, s16
	s_bfe_u32 s16, s28, 0x20003
	s_add_i32 s12, s7, s12
	s_lshr_b32 s11, s11, 26
	s_or_b32 s4, s4, s16
	s_and_b32 s16, s12, 0xf8
	s_add_i32 s11, s8, s11
	s_sub_i32 s7, s7, s16
	s_and_b32 s16, s11, 0xffe0
	s_sub_i32 s8, s8, s16
	s_bfe_i32 s16, s8, 0x80000
	s_bfe_u32 s16, s16, 0x3000c
	s_add_i32 s16, s8, s16
	v_writelane_b32 v253, s17, 23
	s_and_b32 s17, s16, 0xfc
	s_add_i32 s10, s10, s21
	s_sub_i32 s8, s8, s17
	s_ashr_i32 s17, s10, 31
	s_lshr_b32 s17, s17, 22
	s_add_i32 s17, s10, s17
	s_and_b32 s18, s17, 0xfffffc00
	s_sub_i32 s10, s10, s18
	s_ashr_i32 s18, s6, 31
	s_lshr_b32 s18, s18, 29
	s_add_i32 s18, s6, s18
	s_and_b32 s18, s18, -8
	s_sub_i32 s20, s6, s18
	s_bfe_i32 s6, s13, 0x80000
	s_lshl_b64 s[4:5], s[4:5], 10
	s_sext_i32_i16 s6, s6
	v_writelane_b32 v253, s4, 24
	s_sext_i32_i8 s8, s8
	s_ashr_i32 s29, s28, 31
	v_writelane_b32 v253, s5, 25
	s_ashr_i32 s4, s6, 3
	v_writelane_b32 v253, s4, 26
	s_lshr_b32 s4, s6, 3
	s_bfe_i64 s[4:5], s[4:5], 0x100000
	s_lshl_b64 s[4:5], s[4:5], 18
	v_writelane_b32 v253, s4, 27
	s_sext_i32_i8 s6, s7
	s_bfe_i32 s7, s16, 0x80000
	v_writelane_b32 v253, s5, 28
	s_ashr_i32 s4, s9, 5
	s_bfe_i32 s5, s12, 0x80000
	s_lshl_b32 s4, s4, 3
	s_sext_i32_i16 s5, s5
	s_add_i32 s30, s4, s6
	s_ashr_i32 s4, s5, 3
	v_writelane_b32 v253, s4, 29
	s_ashr_i32 s6, s11, 5
	s_sext_i32_i16 s7, s7
	s_lshl_b32 s6, s6, 2
	v_writelane_b32 v253, s21, 30
	s_add_i32 s9, s3, s21
	s_ashr_i32 s3, s7, 2
	s_add_i32 s16, s6, s8
	v_writelane_b32 v253, s3, 31
	s_mov_b32 s8, s28
	v_writelane_b32 v253, s8, 32
	s_lshl_b64 s[28:29], s[28:29], 19
	s_ashr_i32 s31, s30, 31
	v_writelane_b32 v253, s9, 33
	s_ashr_i32 s6, s17, 10
	v_writelane_b32 v253, s28, 34
	s_lshr_b32 s4, s5, 3
	s_lshl_b32 s11, s6, 3
	v_writelane_b32 v253, s29, 35
	s_lshl_b64 s[28:29], s[30:31], 19
	s_sub_i32 s19, s24, s18
	s_bfe_i64 s[4:5], s[4:5], 0x100000
	s_sub_i32 s6, 3, s11
	v_writelane_b32 v253, s28, 36
	s_min_i32 s19, s19, 8
	s_min_u32 s12, s6, 8
	s_lshr_b32 s6, s7, 2
	v_writelane_b32 v253, s29, 37
	s_lshl_b64 s[28:29], s[4:5], 19
	v_writelane_b32 v253, s28, 38
	s_cmp_lt_u32 s9, 16
	v_cvt_f32_i32_e32 v1, s20
	v_writelane_b32 v253, s29, 39
	s_cselect_b64 s[28:29], -1, 0
	v_writelane_b32 v253, s28, 40
	s_ashr_i32 s8, s9, 4
	s_lshl_b32 s3, s9, 18
	v_writelane_b32 v253, s29, 41
	v_writelane_b32 v253, s9, 42
	s_ashr_i32 s9, s8, 31
	s_lshl_b64 s[8:9], s[8:9], 20
	v_writelane_b32 v253, s8, 43
	s_ashr_i32 s27, s26, 31
	s_ashr_i32 s17, s16, 31
	v_writelane_b32 v253, s9, 44
	s_lshl_b64 s[8:9], s[4:5], 18
	v_writelane_b32 v253, s8, 45
	s_lshl_b64 s[4:5], s[4:5], 17
	s_and_b32 s3, s3, 0x3c0000
	v_writelane_b32 v253, s9, 46
	v_writelane_b32 v253, s4, 47
	s_mov_b32 s29, 0
	s_mov_b32 s25, s29
	v_writelane_b32 v253, s5, 48
	s_bfe_i64 s[4:5], s[0:1], 0x100000
	s_lshl_b64 s[4:5], s[4:5], 18
	v_writelane_b32 v253, s4, 49
	s_sext_i32_i16 s0, s19
	v_cvt_f32_i32_e32 v0, s0
	v_writelane_b32 v253, s5, 50
	s_bfe_i64 s[4:5], s[6:7], 0x100000
	s_lshl_b64 s[4:5], s[4:5], 19
	v_writelane_b32 v253, s4, 51
	v_rcp_iflag_f32_e32 v2, v0
	s_mov_b32 s19, 0xf149f2ca
	v_writelane_b32 v253, s5, 52
	s_xor_b32 s4, s20, s0
	s_ashr_i32 s4, s4, 30
	s_or_b32 s6, s4, 1
	v_writelane_b32 v253, s22, 53
	s_lshr_b32 s4, s22, 31
	v_writelane_b32 v253, s4, 54
	s_lshl_b64 s[4:5], s[30:31], 18
	v_writelane_b32 v253, s4, 55
	v_mul_f32_e32 v2, v1, v2
	v_trunc_f32_e32 v2, v2
	v_writelane_b32 v253, s5, 56
	s_mov_b32 s4, s30
	v_writelane_b32 v253, s4, 57
	v_fma_f32 v1, -v2, v0, v1
	s_mov_b32 s22, 0x3d000000
	v_writelane_b32 v253, s5, 58
	s_lshl_b64 s[4:5], s[30:31], 17
	v_writelane_b32 v253, s4, 59
	s_mov_b32 s30, 0xc01d265f
	s_nop 0
	v_writelane_b32 v253, s5, 60
	s_mov_b32 s4, s26
	v_writelane_b32 v253, s4, 61
	s_nop 1
	v_writelane_b32 v253, s5, 62
	s_lshl_b64 s[4:5], s[26:27], 18
	v_writelane_b32 v253, s4, 63
	s_mov_b32 s26, 0x3b800000
	s_nop 0
	v_writelane_b32 v254, s5, 0
	s_mov_b32 s4, s16
	v_writelane_b32 v254, s4, 1
	s_nop 1
	v_writelane_b32 v254, s5, 2
	s_lshl_b64 s[4:5], s[16:17], 19
	v_writelane_b32 v254, s4, 3
	s_mov_b32 s17, 0x800000
	s_mov_b32 s16, 0x3b000000
	v_writelane_b32 v254, s5, 4
	v_cmp_ge_f32_e64 s[4:5], |v1|, |v0|
	v_cvt_i32_f32_e32 v0, v2
	s_and_b64 s[4:5], s[4:5], exec
	s_cselect_b32 s4, s6, 0
	v_cvt_f32_ubyte0_e32 v1, s12
	v_readfirstlane_b32 s5, v0
	s_add_i32 s4, s5, s4
	s_mul_i32 s4, s4, s0
	s_sub_i32 s0, s20, s4
	s_sext_i32_i16 s4, s0
	s_add_i32 s9, s18, s4
	s_ashr_i32 s4, s9, 5
	s_ashr_i32 s5, s4, 31
	s_lshl_b32 s6, s0, 10
	s_and_b32 s8, s6, 0x1c00
	s_lshl_b64 s[6:7], s[4:5], 13
	s_or_b32 s6, s6, s8
	s_bfe_u32 s8, s9, 0x20003
	s_or_b32 s6, s6, s8
	v_cvt_f32_i32_e32 v0, s10
	v_rcp_iflag_f32_e32 v2, v1
	s_lshl_b64 s[6:7], s[6:7], 10
	v_writelane_b32 v254, s6, 5
	s_lshl_b64 s[4:5], s[4:5], 22
	v_mul_f32_e32 v2, v0, v2
	v_writelane_b32 v254, s7, 6
	v_writelane_b32 v254, s4, 7
	v_trunc_f32_e32 v2, v2
	v_fma_f32 v0, -v2, v1, v0
	v_writelane_b32 v254, s5, 8
	s_lshl_b32 s4, s9, 5
	s_and_b32 s6, s4, 0x300
	s_ashr_i32 s4, s10, 30
	s_or_b32 s7, s4, 1
	v_cmp_ge_f32_e64 s[4:5], |v0|, v1
	v_cvt_i32_f32_e32 v0, v2
	s_lshl_b32 s0, s0, 18
	s_and_b32 s0, s0, 0x1c0000
	s_and_b64 s[4:5], s[4:5], exec
	s_cselect_b32 s4, s7, 0
	v_readfirstlane_b32 s5, v0
	s_add_i32 s4, s5, s4
	s_mul_i32 s5, s4, s12
	s_sub_i32 s5, s10, s5
	s_sext_i32_i16 s5, s5
	v_writelane_b32 v254, s9, 9
	s_add_i32 s5, s11, s5
	v_writelane_b32 v254, s5, 10
	s_abs_i32 s5, s2
	v_cvt_f32_u32_e32 v0, s5
	v_writelane_b32 v254, s5, 11
	s_sub_i32 s5, 0, s5
	s_sext_i32_i16 s4, s4
	v_rcp_iflag_f32_e32 v0, v0
	s_lshl_b32 s1, s1, 1
	s_lshl_b32 s0, s0, 1
	s_ashr_i32 s35, s34, 31
	v_mul_f32_e32 v0, 0x4f7ffffe, v0
	v_cvt_u32_f32_e32 v0, v0
	v_mov_b32_e32 v1, 0
	s_add_i32 s31, 0, 0x23600
	s_mov_b32 s18, 0xbd38aa3b
	v_readfirstlane_b32 s7, v0
	s_mul_i32 s5, s5, s7
	s_mul_hi_u32 s5, s7, s5
	s_add_i32 s5, s7, s5
	v_writelane_b32 v254, s5, 12
	v_writelane_b32 v254, s24, 13
	s_nop 1
	v_writelane_b32 v254, s25, 14
	v_writelane_b32 v254, s4, 15
	v_writelane_b32 v254, s1, 16
	v_writelane_b32 v254, s0, 17
	s_lshl_b32 s0, s6, 1
	v_writelane_b32 v254, s0, 18
	s_lshl_b32 s0, s3, 1
	v_writelane_b32 v254, s0, 19
	s_lshl_b32 s0, s88, 7
	v_writelane_b32 v254, s0, 20
	s_lshl_b32 s0, s2, 7
	v_writelane_b32 v254, s0, 21
	s_lshl_b32 s0, s88, 5
	v_writelane_b32 v254, s0, 22
	s_lshl_b32 s0, s2, 5
	v_writelane_b32 v254, s0, 23
	s_add_i32 s0, 0, 0x22000
	v_writelane_b32 v254, s0, 24
	s_add_i32 s0, 0, 0x22004
	v_writelane_b32 v254, s0, 25
	s_add_i32 s0, 0, 0x22d10
	v_writelane_b32 v254, s0, 26
	s_add_i32 s0, 0, 0x22d20
	v_writelane_b32 v254, s0, 27
	s_add_i32 s0, 0, 0x22d30
	v_writelane_b32 v254, s0, 28
	s_add_i32 s0, 0, 0x22d40
	v_writelane_b32 v254, s0, 29
	s_add_i32 s0, 0, 0x22d50
	v_writelane_b32 v254, s0, 30
	s_add_i32 s0, 0, 0x22d60
	v_writelane_b32 v254, s0, 31
	s_add_i32 s0, 0, 0x22d70
	v_writelane_b32 v254, s0, 32
	s_add_i32 s0, 0, 0x22500
	v_writelane_b32 v254, s0, 33
	s_add_i32 s0, 0, 0x23500
	v_writelane_b32 v254, s0, 34
	s_add_i32 s0, 0, 0x22d80
	v_writelane_b32 v254, s0, 35
	s_add_i32 s0, 0, 0x22d90
	v_writelane_b32 v254, s0, 36
	s_add_i32 s0, 0, 0x22da0
	v_writelane_b32 v254, s0, 37
	s_add_i32 s0, 0, 0x22db0
	v_writelane_b32 v254, s0, 38
	s_add_i32 s0, 0, 0x22dc0
	v_writelane_b32 v254, s0, 39
	s_add_i32 s0, 0, 0x22dd0
	v_writelane_b32 v254, s0, 40
	s_add_i32 s0, 0, 0x22de0
	v_writelane_b32 v254, s0, 41
	s_add_i32 s0, 0, 0x22df0
	v_writelane_b32 v254, s0, 42
	s_add_i32 s0, 0, 0x22100
	v_writelane_b32 v254, s0, 43
	s_add_i32 s0, 0, 0x23510
	v_writelane_b32 v254, s0, 44
	s_add_i32 s0, 0, 0x23610
	v_writelane_b32 v254, s0, 45
	s_add_i32 s0, 0, 0x23520
	v_writelane_b32 v254, s0, 46
	s_add_i32 s0, 0, 0x23620
	v_writelane_b32 v254, s0, 47
	s_add_i32 s0, 0, 0x23530
	v_writelane_b32 v254, s0, 48
	s_add_i32 s0, 0, 0x23630
	v_writelane_b32 v254, s0, 49
	s_add_i32 s0, 0, 0x23540
	v_writelane_b32 v254, s0, 50
	s_add_i32 s0, 0, 0x23640
	v_writelane_b32 v254, s0, 51
	s_add_i32 s0, 0, 0x23550
	v_writelane_b32 v254, s0, 52
	s_add_i32 s0, 0, 0x23650
	v_writelane_b32 v254, s0, 53
	s_add_i32 s0, 0, 0x23560
	v_writelane_b32 v254, s0, 54
	s_add_i32 s0, 0, 0x23660
	v_writelane_b32 v254, s0, 55
	s_add_i32 s0, 0, 0x23570
	v_writelane_b32 v254, s0, 56
	s_add_i32 s0, 0, 0x23670
	v_writelane_b32 v254, s0, 57
	s_add_i32 s0, 0, 0x23680
	v_writelane_b32 v254, s0, 58
	s_lshl_b64 s[4:5], s[34:35], 11
	v_writelane_b32 v254, s4, 59
	s_movk_i32 s1, 0x200
	s_add_i32 s3, 0, 0x24a00
	v_writelane_b32 v254, s5, 60
	s_lshl_b64 s[4:5], s[34:35], 10
	v_writelane_b32 v254, s4, 61
	s_mov_b64 s[24:25], 0x80
	s_mov_b32 s0, 0x3e000000
	v_writelane_b32 v254, s5, 62
	s_mov_b32 s4, s88
	v_writelane_b32 v254, s4, 63
	s_mov_b32 s6, s29
	s_nop 0
	v_writelane_b32 v255, s5, 0
	v_writelane_b32 v255, s34, 1
	s_nop 1
	v_writelane_b32 v255, s35, 2
	s_branch .LBB0_193

.LBB0_643:
	s_add_i32 s71, s71, 1
	v_readlane_b32 s4, v253, 5
	v_readlane_b32 s8, v253, 4
	s_mul_i32 s4, s71, s4
	s_mul_hi_u32 s5, s71, s8
	s_add_i32 s5, s5, s4
	s_mul_i32 s4, s71, s8
	v_readlane_b32 s8, v253, 3
	s_add_u32 s10, s4, s8
	v_readlane_b32 s4, v253, 2
	s_addc_u32 s11, s5, s4
	v_readlane_b32 s4, v254, 13
	v_readlane_b32 s5, v254, 14
	s_nop 1
	v_mov_b64_e32 v[2:3], s[4:5]
	v_cmp_ge_i64_e64 s[4:5], s[10:11], v[2:3]
	s_and_b64 vcc, exec, s[4:5]
	s_cbranch_vccnz .LBB0_650
	s_ashr_i32 s8, s10, 31
	s_lshr_b32 s8, s8, 29
	s_add_i32 s8, s10, s8
	s_ashr_i32 s9, s8, 3
	s_and_b32 s8, s8, -8
	s_sub_i32 s8, s10, s8
	s_cmp_lt_i32 s8, 0
	v_readlane_b32 s34, v253, 22
	v_readlane_b32 s35, v253, 23
	s_cselect_b32 s34, s35, s34
	s_mul_i32 s8, s34, s8
	s_add_i32 s8, s8, s9
	s_sub_i32 s8, 0x1ff, s8
	s_ashr_i32 s9, s8, 31
	s_lshr_b32 s9, s9, 29
	s_add_i32 s9, s8, s9
	s_and_b32 s9, s9, -8
	v_readlane_b32 s34, v254, 13
	s_sub_i32 s34, s34, s9
	s_min_i32 s34, s34, 8
	s_abs_i32 s34, s34
	v_cvt_f32_u32_e32 v2, s34
	s_sub_i32 s42, 0, s34
	v_readlane_b32 s35, v254, 14
	s_sub_i32 s8, s8, s9
	v_rcp_iflag_f32_e32 v2, v2
	s_ashr_i32 s35, s8, 31
	s_abs_i32 s8, s8
	v_mul_f32_e32 v2, 0x4f7ffffe, v2
	v_cvt_u32_f32_e32 v2, v2
	s_nop 0
	v_readfirstlane_b32 s43, v2
	s_mul_i32 s42, s42, s43
	s_mul_hi_u32 s42, s43, s42
	s_add_i32 s43, s43, s42
	s_mul_hi_u32 s42, s8, s43
	s_mul_i32 s42, s42, s34
	s_sub_i32 s8, s8, s42
	s_sub_i32 s42, s8, s34
	s_cmp_ge_u32 s8, s34
	s_cselect_b32 s8, s42, s8
	s_sub_i32 s42, s8, s34
	s_cmp_ge_u32 s8, s34
	s_cselect_b32 s8, s42, s8
	s_xor_b32 s8, s8, s35
	s_sub_i32 s8, s8, s35
	s_add_i32 s72, s8, s9
	s_andn2_b64 vcc, exec, s[4:5]
	s_mov_b64 s[8:9], -1
	s_cbranch_vccz .LBB0_651
